# v13
# speedup vs baseline: 1.0054x; 1.0027x over previous
.LBB1_5:
	s_cmp_eq_u32 s45, 0
	s_cselect_b64 s[10:11], -1, 0
	s_cmp_lg_u32 s45, 0
	s_cselect_b64 s[16:17], -1, 0
	s_lshl_b32 s8, s45, 8
	s_add_i32 s21, s23, s8
	s_addk_i32 s21, 0xff00
	s_and_b64 vcc, exec, s[10:11]
	v_mov_b32_e32 v1, v137
	s_cbranch_vccnz .LBB1_7
	v_lshl_add_u32 v0, v130, 2, s21
	ds_read_b32 v1, v0
	s_cmp_eq_u32 s45, 1
	s_cbranch_scc0 .Lnerf_tf0
	ds_read_b32 v168, v0 offset:256
.Lnerf_tf0:
.LBB1_7:
	v_cndmask_b32_e64 v0, 0, 1, s[16:17]
	v_cmp_ne_u32_e64 s[8:9], 1, v0
	s_andn2_b64 vcc, exec, s[16:17]
	v_mov_b32_e32 v0, v139
	s_cbranch_vccnz .LBB1_9
	v_lshl_add_u32 v0, v138, 2, s21
	s_cmp_eq_u32 s45, 1
	s_cbranch_scc0 .Lnerf_tf1
	ds_read_b32 v169, v0 offset:256
.Lnerf_tf1:
	ds_read_b32 v0, v0
.LBB1_9:
	s_waitcnt lgkmcnt(0)
	s_cmp_eq_u32 s45, 2
	s_cbranch_scc0 .Lnerf_do_enc
	v_mov_b32_e32 v208, v148
	v_mov_b32_e32 v209, v149
	v_mov_b32_e32 v210, v150
	v_mov_b32_e32 v211, v151
	v_mov_b32_e32 v212, v168
	v_mov_b32_e32 v213, v169
	v_mov_b32_e32 v214, v170
	v_mov_b32_e32 v215, v171
	v_mov_b32_e32 v216, v172
	v_mov_b32_e32 v217, v173
	v_mov_b32_e32 v218, v174
	v_mov_b32_e32 v219, v175
	v_mov_b32_e32 v220, v176
	v_mov_b32_e32 v221, v177
	v_mov_b32_e32 v222, v178
	v_mov_b32_e32 v223, v179
	s_branch .Lnerf_enc_done
.Lnerf_do_enc:
	v_fma_f32 v2, s18, v1, v127
	v_fma_f32 v3, s22, v1, v128
	v_cndmask_b32_e64 v4, v3, v2, s[4:5]
	v_cndmask_b32_e64 v2, v3, v2, s[6:7]
	v_mul_f32_e32 v8, v2, v142
	v_mul_f32_e32 v2, v2, v143
	v_mul_f32_e32 v5, v4, v140
	v_mul_f32_e32 v4, v4, v141
	v_fract_f32_e32 v2, v2
	v_fract_f32_e32 v4, v4
	v_sin_f32_e32 v10, v2
	v_cos_f32_e32 v2, v2
	v_sin_f32_e32 v7, v4
	v_cos_f32_e32 v4, v4
	v_fma_f32 v1, s26, v1, v129
	v_fract_f32_e32 v5, v5
	v_sin_f32_e32 v6, v5
	v_cos_f32_e32 v5, v5
	v_cndmask_b32_e64 v1, v1, v3, s[2:3]
	v_cvt_pk_bf16_f32 v211, v10, v2
	v_mul_f32_e32 v2, v1, v144
	v_cvt_pk_bf16_f32 v209, v7, v4
	v_fract_f32_e32 v2, v2
	v_mul_f32_e32 v4, v1, v145
	v_sin_f32_e32 v3, v2
	v_cos_f32_e32 v2, v2
	v_fract_f32_e32 v4, v4
	v_cvt_pk_bf16_f32 v208, v6, v5
	v_sin_f32_e32 v5, v4
	v_cos_f32_e32 v4, v4
	v_mul_f32_e32 v6, v1, v146
	v_fract_f32_e32 v6, v6
	v_mul_f32_e32 v1, v1, v147
	v_cos_f32_e32 v7, v6
	v_cvt_pk_bf16_f32 v216, v3, v2
	v_sin_f32_e32 v2, v6
	v_fract_f32_e32 v1, v1
	v_cvt_pk_bf16_f32 v217, v5, v4
	v_cos_f32_e32 v4, v1
	v_sin_f32_e32 v1, v1
	v_cndmask_b32_e64 v3, v7, 0, s[0:1]
	v_cndmask_b32_e64 v2, v2, 1.0, s[0:1]
	v_fract_f32_e32 v8, v8
	v_cvt_pk_bf16_f32 v218, v2, v3
	v_cndmask_b32_e64 v2, v4, 0, s[0:1]
	v_cndmask_b32_e64 v1, v1, 0, s[0:1]
	v_sin_f32_e32 v9, v8
	v_cos_f32_e32 v8, v8
	v_cvt_pk_bf16_f32 v219, v1, v2
	v_fma_f32 v1, s18, v0, v127
	v_fma_f32 v2, s22, v0, v128
	v_cndmask_b32_e64 v3, v2, v1, s[4:5]
	v_cndmask_b32_e64 v1, v2, v1, s[6:7]
	v_mul_f32_e32 v7, v1, v142
	v_mul_f32_e32 v1, v1, v143
	v_mul_f32_e32 v4, v3, v140
	v_mul_f32_e32 v3, v3, v141
	v_fract_f32_e32 v1, v1
	v_cvt_pk_bf16_f32 v210, v9, v8
	v_fract_f32_e32 v3, v3
	v_sin_f32_e32 v9, v1
	v_cos_f32_e32 v1, v1
	v_sin_f32_e32 v6, v3
	v_cos_f32_e32 v3, v3
	v_fma_f32 v0, s26, v0, v129
	v_fract_f32_e32 v4, v4
	v_sin_f32_e32 v5, v4
	v_cos_f32_e32 v4, v4
	v_cndmask_b32_e64 v0, v0, v2, s[2:3]
	v_cvt_pk_bf16_f32 v215, v9, v1
	v_mul_f32_e32 v1, v0, v144
	v_cvt_pk_bf16_f32 v213, v6, v3
	v_fract_f32_e32 v1, v1
	v_mul_f32_e32 v3, v0, v145
	v_sin_f32_e32 v2, v1
	v_cos_f32_e32 v1, v1
	v_fract_f32_e32 v3, v3
	v_cvt_pk_bf16_f32 v212, v5, v4
	v_sin_f32_e32 v4, v3
	v_cos_f32_e32 v3, v3
	v_mul_f32_e32 v5, v0, v146
	v_fract_f32_e32 v5, v5
	v_mul_f32_e32 v0, v0, v147
	v_fract_f32_e32 v7, v7
	v_cos_f32_e32 v6, v5
	v_cvt_pk_bf16_f32 v220, v2, v1
	v_sin_f32_e32 v1, v5
	v_fract_f32_e32 v0, v0
	v_sin_f32_e32 v8, v7
	v_cos_f32_e32 v7, v7
	v_cvt_pk_bf16_f32 v221, v4, v3
	v_cos_f32_e32 v3, v0
	v_cndmask_b32_e64 v2, v6, 0, s[0:1]
	v_cndmask_b32_e64 v1, v1, 1.0, s[0:1]
	v_cvt_pk_bf16_f32 v214, v8, v7
	v_cvt_pk_bf16_f32 v222, v1, v2
	v_sin_f32_e32 v16, v0
	v_cndmask_b32_e64 v17, v3, 0, s[0:1]
	v_cndmask_b32_e64 v16, v16, 0, s[0:1]
	v_cvt_pk_bf16_f32 v223, v16, v17
.Lnerf_enc_done:
	v_mov_b32_e32 v183, v131
	s_mov_b32 s50, 0x10000
	s_mov_b32 s52, 0
	v_or_b32_e32 v88, 0x1a000, v121
	s_waitcnt vmcnt(0) lgkmcnt(0)
	s_barrier
	ds_read_b128 v[224:227], v88 offset:0
	ds_read_b128 v[228:231], v88 offset:1024
	ds_read_b128 v[232:235], v88 offset:2048
	ds_read_b128 v[236:239], v88 offset:3072
	ds_read_b128 v[240:243], v88 offset:4096
	ds_read_b128 v[244:247], v88 offset:5120
	ds_read_b128 v[248:251], v88 offset:6144
	ds_read_b128 v[252:255], v88 offset:7168
	s_waitcnt lgkmcnt(7)
	v_mfma_f32_16x16x32_bf16 v[64:67], v[224:227], v[208:211], 0
	v_mfma_f32_16x16x32_bf16 v[56:59], v[224:227], v[212:215], 0
	ds_read_b128 v[224:227], v88 offset:8192
	s_waitcnt lgkmcnt(7)
	v_mfma_f32_16x16x32_bf16 v[68:71], v[228:231], v[208:211], 0
	v_mfma_f32_16x16x32_bf16 v[60:63], v[228:231], v[212:215], 0
	ds_read_b128 v[228:231], v88 offset:9216
	s_waitcnt lgkmcnt(7)
	v_mfma_f32_16x16x32_bf16 v[64:67], v[232:235], v[216:219], v[64:67]
	v_mfma_f32_16x16x32_bf16 v[56:59], v[232:235], v[220:223], v[56:59]
	ds_read_b128 v[232:235], v88 offset:10240
	s_waitcnt lgkmcnt(7)
	v_mfma_f32_16x16x32_bf16 v[68:71], v[236:239], v[216:219], v[68:71]
	v_mfma_f32_16x16x32_bf16 v[60:63], v[236:239], v[220:223], v[60:63]
	ds_read_b128 v[236:239], v88 offset:11264
	s_waitcnt lgkmcnt(7)
	v_mfma_f32_16x16x32_bf16 v[80:83], v[240:243], v[208:211], 0
	v_cvt_pk_bf16_f32 v0, v64, v65
	v_cvt_pk_bf16_f32 v1, v66, v67
	v_mfma_f32_16x16x32_bf16 v[84:87], v[240:243], v[212:215], 0
	v_cvt_pk_bf16_f32 v4, v56, v57
	v_cvt_pk_bf16_f32 v5, v58, v59
	ds_read_b128 v[240:243], v88 offset:12288
	s_waitcnt lgkmcnt(7)
	v_mfma_f32_16x16x32_bf16 v[76:79], v[244:247], v[208:211], 0
	v_cvt_pk_bf16_f32 v2, v68, v69
	v_cvt_pk_bf16_f32 v3, v70, v71
	s_mov_b32 m0, s28
	s_mov_b32 s51, 0x8000
	v_mfma_f32_16x16x32_bf16 v[72:75], v[244:247], v[212:215], 0
	v_cvt_pk_bf16_f32 v6, v60, v61
	v_cvt_pk_bf16_f32 v7, v62, v63
	buffer_load_dwordx4 v125, s[36:39], s51 offen lds
	ds_read_b128 v[244:247], v88 offset:13312
	s_waitcnt lgkmcnt(7)
	v_mfma_f32_16x16x32_bf16 v[80:83], v[248:251], v[216:219], v[80:83]
	v_pk_max_i16 v0, v0, 0
	v_pk_max_i16 v1, v1, 0
	v_mfma_f32_16x16x32_bf16 v[84:87], v[248:251], v[220:223], v[84:87]
	v_pk_max_i16 v2, v2, 0
	v_pk_max_i16 v3, v3, 0
	ds_read_b128 v[248:251], v88 offset:14336
	s_waitcnt lgkmcnt(7)
	v_mfma_f32_16x16x32_bf16 v[76:79], v[252:255], v[216:219], v[76:79]
	v_pk_max_i16 v4, v4, 0
	v_pk_max_i16 v5, v5, 0
	v_mfma_f32_16x16x32_bf16 v[72:75], v[252:255], v[220:223], v[72:75]
	v_pk_max_i16 v6, v6, 0
	v_pk_max_i16 v7, v7, 0
	ds_read_b128 v[252:255], v88 offset:15360
	s_waitcnt lgkmcnt(7)
	v_mfma_f32_16x16x32_bf16 v[64:67], v[224:227], v[208:211], 0
	v_cvt_pk_bf16_f32 v12, v80, v81
	v_cvt_pk_bf16_f32 v13, v82, v83
	v_mfma_f32_16x16x32_bf16 v[56:59], v[224:227], v[212:215], 0
	v_cvt_pk_bf16_f32 v8, v84, v85
	v_cvt_pk_bf16_f32 v9, v86, v87
	ds_read_b128 v[224:227], v88 offset:16384
	s_waitcnt lgkmcnt(7)
	v_mfma_f32_16x16x32_bf16 v[68:71], v[228:231], v[208:211], 0
	v_cvt_pk_bf16_f32 v14, v76, v77
	v_cvt_pk_bf16_f32 v15, v78, v79
	s_mov_b32 m0, s29
	s_mov_b32 s51, 0xa000
	v_mfma_f32_16x16x32_bf16 v[60:63], v[228:231], v[212:215], 0
	v_cvt_pk_bf16_f32 v10, v72, v73
	v_cvt_pk_bf16_f32 v11, v74, v75
	buffer_load_dwordx4 v125, s[36:39], s51 offen lds
	ds_read_b128 v[228:231], v88 offset:17408
	s_waitcnt lgkmcnt(7)
	v_mfma_f32_16x16x32_bf16 v[64:67], v[232:235], v[216:219], v[64:67]
	v_pk_max_i16 v12, v12, 0
	v_pk_max_i16 v13, v13, 0
	v_mfma_f32_16x16x32_bf16 v[56:59], v[232:235], v[220:223], v[56:59]
	v_pk_max_i16 v14, v14, 0
	v_pk_max_i16 v15, v15, 0
	ds_read_b128 v[232:235], v88 offset:18432
	s_waitcnt lgkmcnt(7)
	v_mfma_f32_16x16x32_bf16 v[68:71], v[236:239], v[216:219], v[68:71]
	v_pk_max_i16 v8, v8, 0
	v_pk_max_i16 v9, v9, 0
	v_mfma_f32_16x16x32_bf16 v[60:63], v[236:239], v[220:223], v[60:63]
	v_pk_max_i16 v10, v10, 0
	v_pk_max_i16 v11, v11, 0
	ds_read_b128 v[236:239], v88 offset:19456
	s_waitcnt lgkmcnt(7)
	v_mfma_f32_16x16x32_bf16 v[80:83], v[240:243], v[208:211], 0
	v_cvt_pk_bf16_f32 v16, v64, v65
	v_cvt_pk_bf16_f32 v17, v66, v67
	v_mfma_f32_16x16x32_bf16 v[84:87], v[240:243], v[212:215], 0
	v_cvt_pk_bf16_f32 v20, v56, v57
	v_cvt_pk_bf16_f32 v21, v58, v59
	ds_read_b128 v[240:243], v88 offset:20480
	s_waitcnt lgkmcnt(7)
	v_mfma_f32_16x16x32_bf16 v[76:79], v[244:247], v[208:211], 0
	v_cvt_pk_bf16_f32 v18, v68, v69
	v_cvt_pk_bf16_f32 v19, v70, v71
	s_mov_b32 m0, s33
	s_mov_b32 s51, 0xc000
	v_mfma_f32_16x16x32_bf16 v[72:75], v[244:247], v[212:215], 0
	v_cvt_pk_bf16_f32 v22, v60, v61
	v_cvt_pk_bf16_f32 v23, v62, v63
	buffer_load_dwordx4 v125, s[36:39], s51 offen lds
	ds_read_b128 v[244:247], v88 offset:21504
	s_waitcnt lgkmcnt(7)
	v_mfma_f32_16x16x32_bf16 v[80:83], v[248:251], v[216:219], v[80:83]
	v_pk_max_i16 v16, v16, 0
	v_pk_max_i16 v17, v17, 0
	v_mfma_f32_16x16x32_bf16 v[84:87], v[248:251], v[220:223], v[84:87]
	v_pk_max_i16 v18, v18, 0
	v_pk_max_i16 v19, v19, 0
	ds_read_b128 v[248:251], v88 offset:22528
	s_waitcnt lgkmcnt(7)
	v_mfma_f32_16x16x32_bf16 v[76:79], v[252:255], v[216:219], v[76:79]
	v_pk_max_i16 v20, v20, 0
	v_pk_max_i16 v21, v21, 0
	v_mfma_f32_16x16x32_bf16 v[72:75], v[252:255], v[220:223], v[72:75]
	v_pk_max_i16 v22, v22, 0
	v_pk_max_i16 v23, v23, 0
	ds_read_b128 v[252:255], v88 offset:23552
	s_waitcnt lgkmcnt(7)
	v_mfma_f32_16x16x32_bf16 v[64:67], v[224:227], v[208:211], 0
	v_cvt_pk_bf16_f32 v24, v80, v81
	v_cvt_pk_bf16_f32 v25, v82, v83
	v_mfma_f32_16x16x32_bf16 v[56:59], v[224:227], v[212:215], 0
	v_cvt_pk_bf16_f32 v28, v84, v85
	v_cvt_pk_bf16_f32 v29, v86, v87
	ds_read_b128 v[224:227], v88 offset:24576
	s_waitcnt lgkmcnt(7)
	v_mfma_f32_16x16x32_bf16 v[68:71], v[228:231], v[208:211], 0
	v_cvt_pk_bf16_f32 v26, v76, v77
	v_cvt_pk_bf16_f32 v27, v78, v79
	s_mov_b32 m0, s34
	s_mov_b32 s51, 0xe000
	v_mfma_f32_16x16x32_bf16 v[60:63], v[228:231], v[212:215], 0
	v_cvt_pk_bf16_f32 v30, v72, v73
	v_cvt_pk_bf16_f32 v31, v74, v75
	buffer_load_dwordx4 v125, s[36:39], s51 offen lds
	ds_read_b128 v[228:231], v88 offset:25600
	s_waitcnt lgkmcnt(7)
	v_mfma_f32_16x16x32_bf16 v[64:67], v[232:235], v[216:219], v[64:67]
	v_pk_max_i16 v24, v24, 0
	v_pk_max_i16 v25, v25, 0
	v_mfma_f32_16x16x32_bf16 v[56:59], v[232:235], v[220:223], v[56:59]
	v_pk_max_i16 v26, v26, 0
	v_pk_max_i16 v27, v27, 0
	ds_read_b128 v[232:235], v88 offset:26624
	s_waitcnt lgkmcnt(7)
	v_mfma_f32_16x16x32_bf16 v[68:71], v[236:239], v[216:219], v[68:71]
	v_pk_max_i16 v28, v28, 0
	v_pk_max_i16 v29, v29, 0
	v_mfma_f32_16x16x32_bf16 v[60:63], v[236:239], v[220:223], v[60:63]
	v_pk_max_i16 v30, v30, 0
	v_pk_max_i16 v31, v31, 0
	ds_read_b128 v[236:239], v88 offset:27648
	s_waitcnt lgkmcnt(7)
	v_mfma_f32_16x16x32_bf16 v[80:83], v[240:243], v[208:211], 0
	v_cvt_pk_bf16_f32 v32, v64, v65
	v_cvt_pk_bf16_f32 v33, v66, v67
	v_mfma_f32_16x16x32_bf16 v[84:87], v[240:243], v[212:215], 0
	v_cvt_pk_bf16_f32 v36, v56, v57
	v_cvt_pk_bf16_f32 v37, v58, v59
	ds_read_b128 v[240:243], v88 offset:28672
	s_waitcnt lgkmcnt(7)
	v_mfma_f32_16x16x32_bf16 v[76:79], v[244:247], v[208:211], 0
	v_cvt_pk_bf16_f32 v34, v68, v69
	v_cvt_pk_bf16_f32 v35, v70, v71
	v_mfma_f32_16x16x32_bf16 v[72:75], v[244:247], v[212:215], 0
	v_cvt_pk_bf16_f32 v38, v60, v61
	v_cvt_pk_bf16_f32 v39, v62, v63
	ds_read_b128 v[244:247], v88 offset:29696
	s_waitcnt lgkmcnt(7)
	v_mfma_f32_16x16x32_bf16 v[80:83], v[248:251], v[216:219], v[80:83]
	v_pk_max_i16 v32, v32, 0
	v_pk_max_i16 v33, v33, 0
	v_mfma_f32_16x16x32_bf16 v[84:87], v[248:251], v[220:223], v[84:87]
	v_pk_max_i16 v34, v34, 0
	v_pk_max_i16 v35, v35, 0
	ds_read_b128 v[248:251], v88 offset:30720
	s_waitcnt lgkmcnt(7)
	v_mfma_f32_16x16x32_bf16 v[76:79], v[252:255], v[216:219], v[76:79]
	v_pk_max_i16 v36, v36, 0
	v_pk_max_i16 v37, v37, 0
	v_mfma_f32_16x16x32_bf16 v[72:75], v[252:255], v[220:223], v[72:75]
	v_pk_max_i16 v38, v38, 0
	v_pk_max_i16 v39, v39, 0
	ds_read_b128 v[252:255], v88 offset:31744
	s_waitcnt lgkmcnt(7)
	v_mfma_f32_16x16x32_bf16 v[64:67], v[224:227], v[208:211], 0
	v_cvt_pk_bf16_f32 v40, v80, v81
	v_cvt_pk_bf16_f32 v41, v82, v83
	v_mfma_f32_16x16x32_bf16 v[56:59], v[224:227], v[212:215], 0
	v_cvt_pk_bf16_f32 v44, v84, v85
	v_cvt_pk_bf16_f32 v45, v86, v87
	s_waitcnt lgkmcnt(6)
	v_mfma_f32_16x16x32_bf16 v[68:71], v[228:231], v[208:211], 0
	v_cvt_pk_bf16_f32 v42, v76, v77
	v_cvt_pk_bf16_f32 v43, v78, v79
	v_mfma_f32_16x16x32_bf16 v[60:63], v[228:231], v[212:215], 0
	v_cvt_pk_bf16_f32 v46, v72, v73
	v_cvt_pk_bf16_f32 v47, v74, v75
	s_waitcnt lgkmcnt(5)
	v_mfma_f32_16x16x32_bf16 v[64:67], v[232:235], v[216:219], v[64:67]
	v_pk_max_i16 v40, v40, 0
	v_pk_max_i16 v41, v41, 0
	v_mfma_f32_16x16x32_bf16 v[56:59], v[232:235], v[220:223], v[56:59]
	v_pk_max_i16 v42, v42, 0
	v_pk_max_i16 v43, v43, 0
	s_waitcnt lgkmcnt(4)
	v_mfma_f32_16x16x32_bf16 v[68:71], v[236:239], v[216:219], v[68:71]
	v_pk_max_i16 v44, v44, 0
	v_pk_max_i16 v45, v45, 0
	v_mfma_f32_16x16x32_bf16 v[60:63], v[236:239], v[220:223], v[60:63]
	v_pk_max_i16 v46, v46, 0
	v_pk_max_i16 v47, v47, 0
	s_cmp_lt_u32 s31, 2
	s_cbranch_scc0 .Lnerf_hid_b_first
	s_waitcnt vmcnt(0) lgkmcnt(0)
	s_barrier
	ds_read_b128 v[224:227], v121 offset:40960
	ds_read_b128 v[228:231], v121 offset:41984
	ds_read_b128 v[152:155], v183 offset:0
	ds_read_b128 v[156:159], v183 offset:64
	v_mfma_f32_16x16x32_bf16 v[80:83], v[240:243], v[208:211], 0
	ds_read_b128 v[232:235], v121 offset:43008
	v_cvt_pk_bf16_f32 v48, v64, v65
	v_cvt_pk_bf16_f32 v49, v66, v67
	v_mfma_f32_16x16x32_bf16 v[84:87], v[240:243], v[212:215], 0
	ds_read_b128 v[236:239], v121 offset:44032
	v_cvt_pk_bf16_f32 v52, v56, v57
	v_cvt_pk_bf16_f32 v53, v58, v59
	ds_read_b128 v[240:243], v121 offset:45056
	v_mfma_f32_16x16x32_bf16 v[76:79], v[244:247], v[208:211], 0
	v_cvt_pk_bf16_f32 v50, v68, v69
	v_cvt_pk_bf16_f32 v51, v70, v71
	v_mfma_f32_16x16x32_bf16 v[72:75], v[244:247], v[212:215], 0
	v_cvt_pk_bf16_f32 v54, v60, v61
	v_cvt_pk_bf16_f32 v55, v62, v63
	ds_read_b128 v[244:247], v121 offset:46080
	v_mfma_f32_16x16x32_bf16 v[80:83], v[248:251], v[216:219], v[80:83]
	v_pk_max_i16 v48, v48, 0
	v_pk_max_i16 v49, v49, 0
	v_mfma_f32_16x16x32_bf16 v[84:87], v[248:251], v[220:223], v[84:87]
	v_pk_max_i16 v50, v50, 0
	v_pk_max_i16 v51, v51, 0
	ds_read_b128 v[248:251], v121 offset:47104
	v_mfma_f32_16x16x32_bf16 v[76:79], v[252:255], v[216:219], v[76:79]
	v_pk_max_i16 v52, v52, 0
	v_pk_max_i16 v53, v53, 0
	v_mfma_f32_16x16x32_bf16 v[72:75], v[252:255], v[220:223], v[72:75]
	v_pk_max_i16 v54, v54, 0
	v_pk_max_i16 v55, v55, 0
	ds_read_b128 v[252:255], v121 offset:48128
	s_setprio 3
	s_waitcnt lgkmcnt(6)
	v_mfma_f32_16x16x32_bf16 v[64:67], v[224:227], v[0:3], v[152:155]
	v_mfma_f32_16x16x32_bf16 v[68:71], v[228:231], v[0:3], v[156:159]
	v_mfma_f32_16x16x32_bf16 v[60:63], v[228:231], v[4:7], v[156:159]
	v_mfma_f32_16x16x32_bf16 v[56:59], v[224:227], v[4:7], v[152:155]
	ds_read_b128 v[224:227], v121 offset:49152
	ds_read_b128 v[228:231], v121 offset:50176
	s_waitcnt lgkmcnt(6)
	ds_read_b128 v[160:163], v183 offset:128
	ds_read_b128 v[164:167], v183 offset:192
	v_mfma_f32_16x16x32_bf16 v[64:67], v[232:235], v[12:15], v[64:67]
	v_cvt_pk_bf16_f32 v112, v80, v81
	v_mfma_f32_16x16x32_bf16 v[68:71], v[236:239], v[12:15], v[68:71]
	s_mov_b32 m0, s35
	s_add_i32 s51, s50, 0x0
	v_cvt_pk_bf16_f32 v113, v82, v83
	v_mfma_f32_16x16x32_bf16 v[60:63], v[236:239], v[8:11], v[60:63]
	buffer_load_dwordx4 v125, s[36:39], s51 offen lds
	v_cvt_pk_bf16_f32 v114, v76, v77
	v_mfma_f32_16x16x32_bf16 v[56:59], v[232:235], v[8:11], v[56:59]
	v_cvt_pk_bf16_f32 v115, v78, v79
	ds_read_b128 v[232:235], v121 offset:51200
	ds_read_b128 v[236:239], v121 offset:52224
	s_waitcnt lgkmcnt(8)
	v_mfma_f32_16x16x32_bf16 v[64:67], v[240:243], v[16:19], v[64:67]
	v_cvt_pk_bf16_f32 v116, v84, v85
	v_mfma_f32_16x16x32_bf16 v[68:71], v[244:247], v[16:19], v[68:71]
	s_mov_b32 m0, s42
	s_add_i32 s51, s50, 0x2000
	v_cvt_pk_bf16_f32 v117, v86, v87
	v_mfma_f32_16x16x32_bf16 v[60:63], v[244:247], v[20:23], v[60:63]
	buffer_load_dwordx4 v125, s[36:39], s51 offen lds
	v_cvt_pk_bf16_f32 v118, v72, v73
	v_mfma_f32_16x16x32_bf16 v[56:59], v[240:243], v[20:23], v[56:59]
	v_cvt_pk_bf16_f32 v119, v74, v75
	ds_read_b128 v[240:243], v121 offset:53248
	ds_read_b128 v[244:247], v121 offset:54272
	s_waitcnt lgkmcnt(8)
	v_mfma_f32_16x16x32_bf16 v[64:67], v[248:251], v[24:27], v[64:67]
	v_pk_max_i16 v112, v112, 0
	v_mfma_f32_16x16x32_bf16 v[68:71], v[252:255], v[24:27], v[68:71]
	s_mov_b32 m0, s41
	s_add_i32 s51, s50, 0x4000
	v_pk_max_i16 v113, v113, 0
	v_mfma_f32_16x16x32_bf16 v[60:63], v[252:255], v[28:31], v[60:63]
	buffer_load_dwordx4 v125, s[36:39], s51 offen lds
	v_pk_max_i16 v114, v114, 0
	v_mfma_f32_16x16x32_bf16 v[56:59], v[248:251], v[28:31], v[56:59]
	v_pk_max_i16 v115, v115, 0
	ds_read_b128 v[248:251], v121 offset:55296
	ds_read_b128 v[252:255], v121 offset:56320
	s_setprio 2
	s_waitcnt lgkmcnt(8)
	v_mfma_f32_16x16x32_bf16 v[64:67], v[224:227], v[32:35], v[64:67]
	v_pk_max_i16 v116, v116, 0
	v_mfma_f32_16x16x32_bf16 v[68:71], v[228:231], v[32:35], v[68:71]
	s_mov_b32 m0, s40
	s_add_i32 s51, s50, 0x6000
	v_pk_max_i16 v117, v117, 0
	v_mfma_f32_16x16x32_bf16 v[60:63], v[228:231], v[36:39], v[60:63]
	buffer_load_dwordx4 v125, s[36:39], s51 offen lds
	v_pk_max_i16 v118, v118, 0
	v_mfma_f32_16x16x32_bf16 v[56:59], v[224:227], v[36:39], v[56:59]
	v_pk_max_i16 v119, v119, 0
	ds_read_b128 v[224:227], v121 offset:57344
	ds_read_b128 v[228:231], v121 offset:58368
	s_waitcnt lgkmcnt(6)
	v_mfma_f32_16x16x32_bf16 v[64:67], v[232:235], v[40:43], v[64:67]
	v_mfma_f32_16x16x32_bf16 v[68:71], v[236:239], v[40:43], v[68:71]
	v_mfma_f32_16x16x32_bf16 v[60:63], v[236:239], v[44:47], v[60:63]
	v_mfma_f32_16x16x32_bf16 v[56:59], v[232:235], v[44:47], v[56:59]
	ds_read_b128 v[232:235], v121 offset:59392
	ds_read_b128 v[236:239], v121 offset:60416
	s_waitcnt lgkmcnt(6)
	ds_read_b128 v[152:155], v183 offset:256
	ds_read_b128 v[156:159], v183 offset:320
	v_mfma_f32_16x16x32_bf16 v[64:67], v[240:243], v[48:51], v[64:67]
	v_mfma_f32_16x16x32_bf16 v[68:71], v[244:247], v[48:51], v[68:71]
	v_mfma_f32_16x16x32_bf16 v[60:63], v[244:247], v[52:55], v[60:63]
	v_mfma_f32_16x16x32_bf16 v[56:59], v[240:243], v[52:55], v[56:59]
	ds_read_b128 v[240:243], v121 offset:61440
	ds_read_b128 v[244:247], v121 offset:62464
	s_waitcnt lgkmcnt(8)
	v_mfma_f32_16x16x32_bf16 v[64:67], v[248:251], v[112:115], v[64:67]
	v_mfma_f32_16x16x32_bf16 v[68:71], v[252:255], v[112:115], v[68:71]
	v_mfma_f32_16x16x32_bf16 v[60:63], v[252:255], v[116:119], v[60:63]
	v_mfma_f32_16x16x32_bf16 v[56:59], v[248:251], v[116:119], v[56:59]
	ds_read_b128 v[248:251], v121 offset:63488
	ds_read_b128 v[252:255], v121 offset:64512
	s_setprio 1
	s_waitcnt lgkmcnt(8)
	v_mfma_f32_16x16x32_bf16 v[80:83], v[224:227], v[0:3], v[160:163]
	v_mfma_f32_16x16x32_bf16 v[76:79], v[228:231], v[0:3], v[164:167]
	v_mfma_f32_16x16x32_bf16 v[72:75], v[228:231], v[4:7], v[164:167]
	v_mfma_f32_16x16x32_bf16 v[84:87], v[224:227], v[4:7], v[160:163]
	ds_read_b128 v[224:227], v126 offset:57344
	ds_read_b128 v[228:231], v126 offset:58368
	s_waitcnt lgkmcnt(8)
	v_mfma_f32_16x16x32_bf16 v[80:83], v[232:235], v[12:15], v[80:83]
	v_cvt_pk_bf16_f32 v88, v64, v65
	v_mfma_f32_16x16x32_bf16 v[76:79], v[236:239], v[12:15], v[76:79]
	v_cvt_pk_bf16_f32 v89, v66, v67
	v_mfma_f32_16x16x32_bf16 v[72:75], v[236:239], v[8:11], v[72:75]
	v_cvt_pk_bf16_f32 v90, v68, v69
	v_mfma_f32_16x16x32_bf16 v[84:87], v[232:235], v[8:11], v[84:87]
	v_cvt_pk_bf16_f32 v91, v70, v71
	ds_read_b128 v[232:235], v126 offset:59392
	ds_read_b128 v[236:239], v126 offset:60416
	s_waitcnt lgkmcnt(6)
	v_mfma_f32_16x16x32_bf16 v[80:83], v[240:243], v[16:19], v[80:83]
	v_cvt_pk_bf16_f32 v92, v56, v57
	v_mfma_f32_16x16x32_bf16 v[76:79], v[244:247], v[16:19], v[76:79]
	v_cvt_pk_bf16_f32 v93, v58, v59
	v_mfma_f32_16x16x32_bf16 v[72:75], v[244:247], v[20:23], v[72:75]
	v_cvt_pk_bf16_f32 v94, v60, v61
	v_mfma_f32_16x16x32_bf16 v[84:87], v[240:243], v[20:23], v[84:87]
	v_cvt_pk_bf16_f32 v95, v62, v63
	ds_read_b128 v[240:243], v126 offset:61440
	ds_read_b128 v[244:247], v126 offset:62464
	s_waitcnt lgkmcnt(6)
	v_mfma_f32_16x16x32_bf16 v[80:83], v[248:251], v[24:27], v[80:83]
	v_pk_max_i16 v88, v88, 0
	v_mfma_f32_16x16x32_bf16 v[76:79], v[252:255], v[24:27], v[76:79]
	v_pk_max_i16 v89, v89, 0
	v_mfma_f32_16x16x32_bf16 v[72:75], v[252:255], v[28:31], v[72:75]
	v_pk_max_i16 v90, v90, 0
	v_mfma_f32_16x16x32_bf16 v[84:87], v[248:251], v[28:31], v[84:87]
	v_pk_max_i16 v91, v91, 0
	ds_read_b128 v[248:251], v126 offset:63488
	ds_read_b128 v[252:255], v126 offset:64512
	s_setprio 0
	s_waitcnt lgkmcnt(6)
	v_mfma_f32_16x16x32_bf16 v[80:83], v[224:227], v[32:35], v[80:83]
	v_pk_max_i16 v92, v92, 0
	v_mfma_f32_16x16x32_bf16 v[76:79], v[228:231], v[32:35], v[76:79]
	v_pk_max_i16 v93, v93, 0
	v_mfma_f32_16x16x32_bf16 v[72:75], v[228:231], v[36:39], v[72:75]
	v_pk_max_i16 v94, v94, 0
	v_mfma_f32_16x16x32_bf16 v[84:87], v[224:227], v[36:39], v[84:87]
	v_pk_max_i16 v95, v95, 0
	s_waitcnt lgkmcnt(4)
	v_mfma_f32_16x16x32_bf16 v[80:83], v[232:235], v[40:43], v[80:83]
	v_mfma_f32_16x16x32_bf16 v[76:79], v[236:239], v[40:43], v[76:79]
	v_mfma_f32_16x16x32_bf16 v[72:75], v[236:239], v[44:47], v[72:75]
	v_mfma_f32_16x16x32_bf16 v[84:87], v[232:235], v[44:47], v[84:87]
	s_branch .Lnerf_hid_a1

.Lnerf_hid_a4:
	s_waitcnt vmcnt(0) lgkmcnt(0)
	s_barrier
	ds_read_b128 v[224:227], v121 offset:40960
	ds_read_b128 v[228:231], v121 offset:41984
	v_mfma_f32_16x16x32_bf16 v[80:83], v[240:243], v[48:51], v[80:83]
	ds_read_b128 v[232:235], v121 offset:43008
	v_mfma_f32_16x16x32_bf16 v[76:79], v[244:247], v[48:51], v[76:79]
	ds_read_b128 v[236:239], v121 offset:44032
	v_mfma_f32_16x16x32_bf16 v[72:75], v[244:247], v[52:55], v[72:75]
	v_mfma_f32_16x16x32_bf16 v[84:87], v[240:243], v[52:55], v[84:87]
	ds_read_b128 v[240:243], v121 offset:45056
	ds_read_b128 v[244:247], v121 offset:46080
	v_mfma_f32_16x16x32_bf16 v[80:83], v[248:251], v[112:115], v[80:83]
	v_mfma_f32_16x16x32_bf16 v[76:79], v[252:255], v[112:115], v[76:79]
	v_mfma_f32_16x16x32_bf16 v[72:75], v[252:255], v[116:119], v[72:75]
	v_mfma_f32_16x16x32_bf16 v[84:87], v[248:251], v[116:119], v[84:87]
	ds_read_b128 v[248:251], v121 offset:47104
	ds_read_b128 v[252:255], v121 offset:48128
	s_setprio 3
	s_waitcnt lgkmcnt(6)
	v_mfma_f32_16x16x32_bf16 v[64:67], v[224:227], v[88:91], v[152:155]
	v_mfma_f32_16x16x32_bf16 v[68:71], v[228:231], v[88:91], v[156:159]
	v_mfma_f32_16x16x32_bf16 v[60:63], v[228:231], v[92:95], v[156:159]
	v_mfma_f32_16x16x32_bf16 v[56:59], v[224:227], v[92:95], v[152:155]
	ds_read_b128 v[224:227], v121 offset:49152
	ds_read_b128 v[228:231], v121 offset:50176
	s_lshl_b32 s56, s45, 4
	s_or_b32 s56, s56, s52
	s_cmp_eq_u32 s56, 0x10
	s_cbranch_scc0 .Lnerf_e2skip_1
	v_mov_b32_e32 v1, v168
	v_mov_b32_e32 v0, v169
	v_fma_f32 v2, s18, v1, v127
	v_fma_f32 v3, s22, v1, v128
	v_cndmask_b32_e64 v4, v3, v2, s[4:5]
	v_cndmask_b32_e64 v2, v3, v2, s[6:7]
	v_mul_f32_e32 v8, v2, v142
	v_mul_f32_e32 v2, v2, v143
	v_mul_f32_e32 v5, v4, v140
	v_mul_f32_e32 v4, v4, v141
	v_fract_f32_e32 v2, v2
	v_fract_f32_e32 v4, v4
	v_sin_f32_e32 v10, v2
	v_cos_f32_e32 v2, v2
	v_sin_f32_e32 v7, v4
	v_cos_f32_e32 v4, v4
	v_fma_f32 v1, s26, v1, v129
	v_fract_f32_e32 v5, v5
	v_sin_f32_e32 v6, v5
	v_cos_f32_e32 v5, v5
	v_cndmask_b32_e64 v1, v1, v3, s[2:3]
	v_cvt_pk_bf16_f32 v151, v10, v2
	v_mul_f32_e32 v2, v1, v144
	v_cvt_pk_bf16_f32 v149, v7, v4
	v_fract_f32_e32 v2, v2
	v_mul_f32_e32 v4, v1, v145
	v_sin_f32_e32 v3, v2
	v_cos_f32_e32 v2, v2
	v_fract_f32_e32 v4, v4
	v_cvt_pk_bf16_f32 v148, v6, v5
	v_sin_f32_e32 v5, v4
	v_cos_f32_e32 v4, v4
	v_mul_f32_e32 v6, v1, v146
	v_fract_f32_e32 v6, v6
	v_mul_f32_e32 v1, v1, v147
	v_cos_f32_e32 v7, v6
	v_cvt_pk_bf16_f32 v172, v3, v2
	v_sin_f32_e32 v2, v6
	v_fract_f32_e32 v1, v1
	v_cvt_pk_bf16_f32 v173, v5, v4
	v_cos_f32_e32 v4, v1
	v_sin_f32_e32 v1, v1
	v_cndmask_b32_e64 v3, v7, 0, s[0:1]
	v_cndmask_b32_e64 v2, v2, 1.0, s[0:1]
	v_fract_f32_e32 v8, v8
	v_cvt_pk_bf16_f32 v174, v2, v3
	v_cndmask_b32_e64 v2, v4, 0, s[0:1]
	v_cndmask_b32_e64 v1, v1, 0, s[0:1]
	v_sin_f32_e32 v9, v8
	v_cos_f32_e32 v8, v8
	v_cvt_pk_bf16_f32 v175, v1, v2
	v_fma_f32 v1, s18, v0, v127
	v_fma_f32 v2, s22, v0, v128
	v_cndmask_b32_e64 v3, v2, v1, s[4:5]
	v_cndmask_b32_e64 v1, v2, v1, s[6:7]
	v_mul_f32_e32 v7, v1, v142
	v_mul_f32_e32 v1, v1, v143
	v_mul_f32_e32 v4, v3, v140
	v_mul_f32_e32 v3, v3, v141
	v_fract_f32_e32 v1, v1
	v_cvt_pk_bf16_f32 v150, v9, v8
	v_fract_f32_e32 v3, v3
	v_sin_f32_e32 v9, v1
	v_cos_f32_e32 v1, v1
	v_sin_f32_e32 v6, v3
	v_cos_f32_e32 v3, v3
	v_fma_f32 v0, s26, v0, v129
	v_fract_f32_e32 v4, v4
	v_sin_f32_e32 v5, v4
	v_cos_f32_e32 v4, v4
	v_cndmask_b32_e64 v0, v0, v2, s[2:3]
	v_cvt_pk_bf16_f32 v171, v9, v1
	v_mul_f32_e32 v1, v0, v144
	v_cvt_pk_bf16_f32 v169, v6, v3
	v_fract_f32_e32 v1, v1
	v_mul_f32_e32 v3, v0, v145
	v_sin_f32_e32 v2, v1
	v_cos_f32_e32 v1, v1
	v_fract_f32_e32 v3, v3
	v_cvt_pk_bf16_f32 v168, v5, v4
	v_sin_f32_e32 v4, v3
	v_cos_f32_e32 v3, v3
	v_mul_f32_e32 v5, v0, v146
	v_fract_f32_e32 v5, v5
	v_mul_f32_e32 v0, v0, v147
	v_fract_f32_e32 v7, v7
	v_cos_f32_e32 v6, v5
	v_cvt_pk_bf16_f32 v176, v2, v1
	v_sin_f32_e32 v1, v5
	v_fract_f32_e32 v0, v0
	v_sin_f32_e32 v8, v7
	v_cos_f32_e32 v7, v7
	v_cvt_pk_bf16_f32 v177, v4, v3
	v_cos_f32_e32 v3, v0
	v_cndmask_b32_e64 v2, v6, 0, s[0:1]
	v_cndmask_b32_e64 v1, v1, 1.0, s[0:1]
	v_cvt_pk_bf16_f32 v170, v8, v7
	v_cvt_pk_bf16_f32 v178, v1, v2
	v_sin_f32_e32 v16, v0
	v_cndmask_b32_e64 v17, v3, 0, s[0:1]
	v_cndmask_b32_e64 v16, v16, 0, s[0:1]
	v_cvt_pk_bf16_f32 v179, v16, v17
.Lnerf_e2skip_1:
	s_waitcnt lgkmcnt(6)
	ds_read_b128 v[160:163], v183 offset:1152
	ds_read_b128 v[164:167], v183 offset:1216
	v_mfma_f32_16x16x32_bf16 v[64:67], v[232:235], v[96:99], v[64:67]
	v_mfma_f32_16x16x32_bf16 v[68:71], v[236:239], v[96:99], v[68:71]
	s_mov_b32 m0, s35
	s_add_i32 s51, s50, 0x20000
	v_mfma_f32_16x16x32_bf16 v[60:63], v[236:239], v[100:103], v[60:63]
	buffer_load_dwordx4 v125, s[36:39], s51 offen lds
	v_mfma_f32_16x16x32_bf16 v[56:59], v[232:235], v[100:103], v[56:59]
	ds_read_b128 v[232:235], v121 offset:51200
	ds_read_b128 v[236:239], v121 offset:52224
	s_waitcnt lgkmcnt(8)
	v_mfma_f32_16x16x32_bf16 v[64:67], v[240:243], v[104:107], v[64:67]
	v_mfma_f32_16x16x32_bf16 v[68:71], v[244:247], v[104:107], v[68:71]
	s_mov_b32 m0, s42
	s_add_i32 s51, s50, 0x22000
	v_mfma_f32_16x16x32_bf16 v[60:63], v[244:247], v[108:111], v[60:63]
	buffer_load_dwordx4 v125, s[36:39], s51 offen lds
	v_mfma_f32_16x16x32_bf16 v[56:59], v[240:243], v[108:111], v[56:59]
	ds_read_b128 v[240:243], v121 offset:53248
	ds_read_b128 v[244:247], v121 offset:54272
	s_waitcnt lgkmcnt(8)
	v_mfma_f32_16x16x32_bf16 v[64:67], v[248:251], v[184:187], v[64:67]
	v_cvt_pk_bf16_f32 v216, v80, v81
	v_mfma_f32_16x16x32_bf16 v[68:71], v[252:255], v[184:187], v[68:71]
	s_mov_b32 m0, s41
	s_add_i32 s51, s50, 0x24000
	v_cvt_pk_bf16_f32 v217, v82, v83
	v_mfma_f32_16x16x32_bf16 v[60:63], v[252:255], v[188:191], v[60:63]
	buffer_load_dwordx4 v125, s[36:39], s51 offen lds
	v_cvt_pk_bf16_f32 v218, v76, v77
	v_mfma_f32_16x16x32_bf16 v[56:59], v[248:251], v[188:191], v[56:59]
	v_cvt_pk_bf16_f32 v219, v78, v79
	ds_read_b128 v[248:251], v121 offset:55296
	ds_read_b128 v[252:255], v121 offset:56320
	s_setprio 2
	s_waitcnt lgkmcnt(8)
	v_mfma_f32_16x16x32_bf16 v[64:67], v[224:227], v[192:195], v[64:67]
	v_cvt_pk_bf16_f32 v220, v84, v85
	v_mfma_f32_16x16x32_bf16 v[68:71], v[228:231], v[192:195], v[68:71]
	s_mov_b32 m0, s40
	s_add_i32 s51, s50, 0x26000
	v_cvt_pk_bf16_f32 v221, v86, v87
	v_mfma_f32_16x16x32_bf16 v[60:63], v[228:231], v[196:199], v[60:63]
	buffer_load_dwordx4 v125, s[36:39], s51 offen lds
	v_cvt_pk_bf16_f32 v222, v72, v73
	v_mfma_f32_16x16x32_bf16 v[56:59], v[224:227], v[196:199], v[56:59]
	v_cvt_pk_bf16_f32 v223, v74, v75
	ds_read_b128 v[224:227], v121 offset:57344
	ds_read_b128 v[228:231], v121 offset:58368
	s_waitcnt lgkmcnt(6)
	v_mfma_f32_16x16x32_bf16 v[64:67], v[232:235], v[200:203], v[64:67]
	v_pk_max_i16 v216, v216, 0
	v_mfma_f32_16x16x32_bf16 v[68:71], v[236:239], v[200:203], v[68:71]
	v_pk_max_i16 v217, v217, 0
	v_mfma_f32_16x16x32_bf16 v[60:63], v[236:239], v[204:207], v[60:63]
	v_pk_max_i16 v218, v218, 0
	v_mfma_f32_16x16x32_bf16 v[56:59], v[232:235], v[204:207], v[56:59]
	v_pk_max_i16 v219, v219, 0
	ds_read_b128 v[232:235], v121 offset:59392
	ds_read_b128 v[236:239], v121 offset:60416
	s_waitcnt lgkmcnt(6)
	ds_read_b128 v[152:155], v183 offset:1280
	ds_read_b128 v[156:159], v183 offset:1344
	v_mfma_f32_16x16x32_bf16 v[64:67], v[240:243], v[208:211], v[64:67]
	v_pk_max_i16 v220, v220, 0
	v_mfma_f32_16x16x32_bf16 v[68:71], v[244:247], v[208:211], v[68:71]
	v_pk_max_i16 v221, v221, 0
	v_mfma_f32_16x16x32_bf16 v[60:63], v[244:247], v[212:215], v[60:63]
	v_pk_max_i16 v222, v222, 0
	v_mfma_f32_16x16x32_bf16 v[56:59], v[240:243], v[212:215], v[56:59]
	v_pk_max_i16 v223, v223, 0
	ds_read_b128 v[240:243], v121 offset:61440
	ds_read_b128 v[244:247], v121 offset:62464
	s_waitcnt lgkmcnt(8)
	v_mfma_f32_16x16x32_bf16 v[64:67], v[248:251], v[216:219], v[64:67]
	v_mfma_f32_16x16x32_bf16 v[68:71], v[252:255], v[216:219], v[68:71]
	v_mfma_f32_16x16x32_bf16 v[60:63], v[252:255], v[220:223], v[60:63]
	v_mfma_f32_16x16x32_bf16 v[56:59], v[248:251], v[220:223], v[56:59]
	ds_read_b128 v[248:251], v121 offset:63488
	ds_read_b128 v[252:255], v121 offset:64512
	s_setprio 1
	s_waitcnt lgkmcnt(8)
	v_mfma_f32_16x16x32_bf16 v[80:83], v[224:227], v[88:91], v[160:163]
	v_mfma_f32_16x16x32_bf16 v[76:79], v[228:231], v[88:91], v[164:167]
	v_mfma_f32_16x16x32_bf16 v[72:75], v[228:231], v[92:95], v[164:167]
	v_mfma_f32_16x16x32_bf16 v[84:87], v[224:227], v[92:95], v[160:163]
	ds_read_b128 v[224:227], v126 offset:57344
	ds_read_b128 v[228:231], v126 offset:58368
	s_waitcnt lgkmcnt(8)
	v_mfma_f32_16x16x32_bf16 v[80:83], v[232:235], v[96:99], v[80:83]
	v_cvt_pk_bf16_f32 v0, v64, v65
	v_mfma_f32_16x16x32_bf16 v[76:79], v[236:239], v[96:99], v[76:79]
	v_cvt_pk_bf16_f32 v1, v66, v67
	v_mfma_f32_16x16x32_bf16 v[72:75], v[236:239], v[100:103], v[72:75]
	v_cvt_pk_bf16_f32 v2, v68, v69
	v_mfma_f32_16x16x32_bf16 v[84:87], v[232:235], v[100:103], v[84:87]
	v_cvt_pk_bf16_f32 v3, v70, v71
	ds_read_b128 v[232:235], v126 offset:59392
	ds_read_b128 v[236:239], v126 offset:60416
	s_waitcnt lgkmcnt(6)
	v_mfma_f32_16x16x32_bf16 v[80:83], v[240:243], v[104:107], v[80:83]
	v_cvt_pk_bf16_f32 v4, v56, v57
	v_mfma_f32_16x16x32_bf16 v[76:79], v[244:247], v[104:107], v[76:79]
	v_cvt_pk_bf16_f32 v5, v58, v59
	v_mfma_f32_16x16x32_bf16 v[72:75], v[244:247], v[108:111], v[72:75]
	v_cvt_pk_bf16_f32 v6, v60, v61
	v_mfma_f32_16x16x32_bf16 v[84:87], v[240:243], v[108:111], v[84:87]
	v_cvt_pk_bf16_f32 v7, v62, v63
	ds_read_b128 v[240:243], v126 offset:61440
	ds_read_b128 v[244:247], v126 offset:62464
	s_waitcnt lgkmcnt(6)
	v_mfma_f32_16x16x32_bf16 v[80:83], v[248:251], v[184:187], v[80:83]
	v_pk_max_i16 v0, v0, 0
	v_mfma_f32_16x16x32_bf16 v[76:79], v[252:255], v[184:187], v[76:79]
	v_pk_max_i16 v1, v1, 0
	v_mfma_f32_16x16x32_bf16 v[72:75], v[252:255], v[188:191], v[72:75]
	v_pk_max_i16 v2, v2, 0
	v_mfma_f32_16x16x32_bf16 v[84:87], v[248:251], v[188:191], v[84:87]
	v_pk_max_i16 v3, v3, 0
	ds_read_b128 v[248:251], v126 offset:63488
	ds_read_b128 v[252:255], v126 offset:64512
	s_setprio 0
	s_waitcnt lgkmcnt(6)
	v_mfma_f32_16x16x32_bf16 v[80:83], v[224:227], v[192:195], v[80:83]
	v_pk_max_i16 v4, v4, 0
	v_mfma_f32_16x16x32_bf16 v[76:79], v[228:231], v[192:195], v[76:79]
	v_pk_max_i16 v5, v5, 0
	v_mfma_f32_16x16x32_bf16 v[72:75], v[228:231], v[196:199], v[72:75]
	v_pk_max_i16 v6, v6, 0
	v_mfma_f32_16x16x32_bf16 v[84:87], v[224:227], v[196:199], v[84:87]
	v_pk_max_i16 v7, v7, 0
	s_waitcnt lgkmcnt(4)
	v_mfma_f32_16x16x32_bf16 v[80:83], v[232:235], v[200:203], v[80:83]
	v_mfma_f32_16x16x32_bf16 v[76:79], v[236:239], v[200:203], v[76:79]
	v_mfma_f32_16x16x32_bf16 v[72:75], v[236:239], v[204:207], v[72:75]
	v_mfma_f32_16x16x32_bf16 v[84:87], v[232:235], v[204:207], v[84:87]

.Lnerf_hid_b4:
	s_waitcnt vmcnt(0) lgkmcnt(0)
	s_barrier
	ds_read_b128 v[224:227], v121 offset:40960
	ds_read_b128 v[228:231], v121 offset:41984
	v_mfma_f32_16x16x32_bf16 v[80:83], v[240:243], v[48:51], v[80:83]
	ds_read_b128 v[232:235], v121 offset:43008
	v_mfma_f32_16x16x32_bf16 v[76:79], v[244:247], v[48:51], v[76:79]
	ds_read_b128 v[236:239], v121 offset:44032
	v_mfma_f32_16x16x32_bf16 v[72:75], v[244:247], v[52:55], v[72:75]
	v_mfma_f32_16x16x32_bf16 v[84:87], v[240:243], v[52:55], v[84:87]
	ds_read_b128 v[240:243], v121 offset:45056
	ds_read_b128 v[244:247], v121 offset:46080
	v_mfma_f32_16x16x32_bf16 v[80:83], v[248:251], v[112:115], v[80:83]
	v_mfma_f32_16x16x32_bf16 v[76:79], v[252:255], v[112:115], v[76:79]
	v_mfma_f32_16x16x32_bf16 v[72:75], v[252:255], v[116:119], v[72:75]
	v_mfma_f32_16x16x32_bf16 v[84:87], v[248:251], v[116:119], v[84:87]
	ds_read_b128 v[248:251], v121 offset:47104
	ds_read_b128 v[252:255], v121 offset:48128
	s_setprio 3
	s_waitcnt lgkmcnt(6)
	v_mfma_f32_16x16x32_bf16 v[64:67], v[224:227], v[88:91], v[152:155]
	v_mfma_f32_16x16x32_bf16 v[68:71], v[228:231], v[88:91], v[156:159]
	v_mfma_f32_16x16x32_bf16 v[60:63], v[228:231], v[92:95], v[156:159]
	v_mfma_f32_16x16x32_bf16 v[56:59], v[224:227], v[92:95], v[152:155]
	ds_read_b128 v[224:227], v121 offset:49152
	ds_read_b128 v[228:231], v121 offset:50176
	s_lshl_b32 s56, s45, 4
	s_or_b32 s56, s56, s52
	s_cmp_eq_u32 s56, 0x11
	s_cbranch_scc0 .Lnerf_e2skip_2
	v_mov_b32_e32 v1, v168
	v_mov_b32_e32 v0, v169
	v_fma_f32 v2, s18, v1, v127
	v_fma_f32 v3, s22, v1, v128
	v_cndmask_b32_e64 v4, v3, v2, s[4:5]
	v_cndmask_b32_e64 v2, v3, v2, s[6:7]
	v_mul_f32_e32 v8, v2, v142
	v_mul_f32_e32 v2, v2, v143
	v_mul_f32_e32 v5, v4, v140
	v_mul_f32_e32 v4, v4, v141
	v_fract_f32_e32 v2, v2
	v_fract_f32_e32 v4, v4
	v_sin_f32_e32 v10, v2
	v_cos_f32_e32 v2, v2
	v_sin_f32_e32 v7, v4
	v_cos_f32_e32 v4, v4
	v_fma_f32 v1, s26, v1, v129
	v_fract_f32_e32 v5, v5
	v_sin_f32_e32 v6, v5
	v_cos_f32_e32 v5, v5
	v_cndmask_b32_e64 v1, v1, v3, s[2:3]
	v_cvt_pk_bf16_f32 v151, v10, v2
	v_mul_f32_e32 v2, v1, v144
	v_cvt_pk_bf16_f32 v149, v7, v4
	v_fract_f32_e32 v2, v2
	v_mul_f32_e32 v4, v1, v145
	v_sin_f32_e32 v3, v2
	v_cos_f32_e32 v2, v2
	v_fract_f32_e32 v4, v4
	v_cvt_pk_bf16_f32 v148, v6, v5
	v_sin_f32_e32 v5, v4
	v_cos_f32_e32 v4, v4
	v_mul_f32_e32 v6, v1, v146
	v_fract_f32_e32 v6, v6
	v_mul_f32_e32 v1, v1, v147
	v_cos_f32_e32 v7, v6
	v_cvt_pk_bf16_f32 v172, v3, v2
	v_sin_f32_e32 v2, v6
	v_fract_f32_e32 v1, v1
	v_cvt_pk_bf16_f32 v173, v5, v4
	v_cos_f32_e32 v4, v1
	v_sin_f32_e32 v1, v1
	v_cndmask_b32_e64 v3, v7, 0, s[0:1]
	v_cndmask_b32_e64 v2, v2, 1.0, s[0:1]
	v_fract_f32_e32 v8, v8
	v_cvt_pk_bf16_f32 v174, v2, v3
	v_cndmask_b32_e64 v2, v4, 0, s[0:1]
	v_cndmask_b32_e64 v1, v1, 0, s[0:1]
	v_sin_f32_e32 v9, v8
	v_cos_f32_e32 v8, v8
	v_cvt_pk_bf16_f32 v175, v1, v2
	v_fma_f32 v1, s18, v0, v127
	v_fma_f32 v2, s22, v0, v128
	v_cndmask_b32_e64 v3, v2, v1, s[4:5]
	v_cndmask_b32_e64 v1, v2, v1, s[6:7]
	v_mul_f32_e32 v7, v1, v142
	v_mul_f32_e32 v1, v1, v143
	v_mul_f32_e32 v4, v3, v140
	v_mul_f32_e32 v3, v3, v141
	v_fract_f32_e32 v1, v1
	v_cvt_pk_bf16_f32 v150, v9, v8
	v_fract_f32_e32 v3, v3
	v_sin_f32_e32 v9, v1
	v_cos_f32_e32 v1, v1
	v_sin_f32_e32 v6, v3
	v_cos_f32_e32 v3, v3
	v_fma_f32 v0, s26, v0, v129
	v_fract_f32_e32 v4, v4
	v_sin_f32_e32 v5, v4
	v_cos_f32_e32 v4, v4
	v_cndmask_b32_e64 v0, v0, v2, s[2:3]
	v_cvt_pk_bf16_f32 v171, v9, v1
	v_mul_f32_e32 v1, v0, v144
	v_cvt_pk_bf16_f32 v169, v6, v3
	v_fract_f32_e32 v1, v1
	v_mul_f32_e32 v3, v0, v145
	v_sin_f32_e32 v2, v1
	v_cos_f32_e32 v1, v1
	v_fract_f32_e32 v3, v3
	v_cvt_pk_bf16_f32 v168, v5, v4
	v_sin_f32_e32 v4, v3
	v_cos_f32_e32 v3, v3
	v_mul_f32_e32 v5, v0, v146
	v_fract_f32_e32 v5, v5
	v_mul_f32_e32 v0, v0, v147
	v_fract_f32_e32 v7, v7
	v_cos_f32_e32 v6, v5
	v_cvt_pk_bf16_f32 v176, v2, v1
	v_sin_f32_e32 v1, v5
	v_fract_f32_e32 v0, v0
	v_sin_f32_e32 v8, v7
	v_cos_f32_e32 v7, v7
	v_cvt_pk_bf16_f32 v177, v4, v3
	v_cos_f32_e32 v3, v0
	v_cndmask_b32_e64 v2, v6, 0, s[0:1]
	v_cndmask_b32_e64 v1, v1, 1.0, s[0:1]
	v_cvt_pk_bf16_f32 v170, v8, v7
	v_cvt_pk_bf16_f32 v178, v1, v2
	v_sin_f32_e32 v16, v0
	v_cndmask_b32_e64 v17, v3, 0, s[0:1]
	v_cndmask_b32_e64 v16, v16, 0, s[0:1]
	v_cvt_pk_bf16_f32 v179, v16, v17
.Lnerf_e2skip_2:
	s_waitcnt lgkmcnt(6)
	ds_read_b128 v[160:163], v183 offset:1152
	ds_read_b128 v[164:167], v183 offset:1216
	v_mfma_f32_16x16x32_bf16 v[64:67], v[232:235], v[96:99], v[64:67]
	v_cvt_pk_bf16_f32 v216, v80, v81
	v_mfma_f32_16x16x32_bf16 v[68:71], v[236:239], v[96:99], v[68:71]
	v_cvt_pk_bf16_f32 v217, v82, v83
	v_mfma_f32_16x16x32_bf16 v[60:63], v[236:239], v[100:103], v[60:63]
	v_cvt_pk_bf16_f32 v218, v76, v77
	v_mfma_f32_16x16x32_bf16 v[56:59], v[232:235], v[100:103], v[56:59]
	v_cvt_pk_bf16_f32 v219, v78, v79
	ds_read_b128 v[232:235], v121 offset:51200
	ds_read_b128 v[236:239], v121 offset:52224
	s_waitcnt lgkmcnt(8)
	v_mfma_f32_16x16x32_bf16 v[64:67], v[240:243], v[104:107], v[64:67]
	v_cvt_pk_bf16_f32 v220, v84, v85
	v_mfma_f32_16x16x32_bf16 v[68:71], v[244:247], v[104:107], v[68:71]
	v_cvt_pk_bf16_f32 v221, v86, v87
	v_mfma_f32_16x16x32_bf16 v[60:63], v[244:247], v[108:111], v[60:63]
	v_cvt_pk_bf16_f32 v222, v72, v73
	v_mfma_f32_16x16x32_bf16 v[56:59], v[240:243], v[108:111], v[56:59]
	v_cvt_pk_bf16_f32 v223, v74, v75
	ds_read_b128 v[240:243], v121 offset:53248
	ds_read_b128 v[244:247], v121 offset:54272
	s_waitcnt lgkmcnt(8)
	v_mfma_f32_16x16x32_bf16 v[64:67], v[248:251], v[184:187], v[64:67]
	v_pk_max_i16 v216, v216, 0
	v_mfma_f32_16x16x32_bf16 v[68:71], v[252:255], v[184:187], v[68:71]
	v_pk_max_i16 v217, v217, 0
	v_mfma_f32_16x16x32_bf16 v[60:63], v[252:255], v[188:191], v[60:63]
	v_pk_max_i16 v218, v218, 0
	v_mfma_f32_16x16x32_bf16 v[56:59], v[248:251], v[188:191], v[56:59]
	v_pk_max_i16 v219, v219, 0
	ds_read_b128 v[248:251], v121 offset:55296
	ds_read_b128 v[252:255], v121 offset:56320
	s_setprio 2
	s_waitcnt lgkmcnt(8)
	v_mfma_f32_16x16x32_bf16 v[64:67], v[224:227], v[192:195], v[64:67]
	v_pk_max_i16 v220, v220, 0
	v_mfma_f32_16x16x32_bf16 v[68:71], v[228:231], v[192:195], v[68:71]
	v_pk_max_i16 v221, v221, 0
	v_mfma_f32_16x16x32_bf16 v[60:63], v[228:231], v[196:199], v[60:63]
	v_pk_max_i16 v222, v222, 0
	v_mfma_f32_16x16x32_bf16 v[56:59], v[224:227], v[196:199], v[56:59]
	v_pk_max_i16 v223, v223, 0
	ds_read_b128 v[224:227], v121 offset:57344
	ds_read_b128 v[228:231], v121 offset:58368
	s_waitcnt lgkmcnt(6)
	v_mfma_f32_16x16x32_bf16 v[64:67], v[232:235], v[200:203], v[64:67]
	v_mfma_f32_16x16x32_bf16 v[68:71], v[236:239], v[200:203], v[68:71]
	s_mov_b32 m0, s35
	s_add_i32 s51, s50, 0x20000
	v_mfma_f32_16x16x32_bf16 v[60:63], v[236:239], v[204:207], v[60:63]
	buffer_load_dwordx4 v125, s[36:39], s51 offen lds
	v_mfma_f32_16x16x32_bf16 v[56:59], v[232:235], v[204:207], v[56:59]
	ds_read_b128 v[232:235], v121 offset:59392
	ds_read_b128 v[236:239], v121 offset:60416
	s_waitcnt lgkmcnt(6)
	ds_read_b128 v[152:155], v183 offset:1280
	ds_read_b128 v[156:159], v183 offset:1344
	v_mfma_f32_16x16x32_bf16 v[64:67], v[240:243], v[208:211], v[64:67]
	v_mfma_f32_16x16x32_bf16 v[68:71], v[244:247], v[208:211], v[68:71]
	s_mov_b32 m0, s42
	s_add_i32 s51, s50, 0x22000
	v_mfma_f32_16x16x32_bf16 v[60:63], v[244:247], v[212:215], v[60:63]
	buffer_load_dwordx4 v125, s[36:39], s51 offen lds
	v_mfma_f32_16x16x32_bf16 v[56:59], v[240:243], v[212:215], v[56:59]
	ds_read_b128 v[240:243], v121 offset:61440
	ds_read_b128 v[244:247], v121 offset:62464
	s_waitcnt lgkmcnt(8)
	v_mfma_f32_16x16x32_bf16 v[64:67], v[248:251], v[216:219], v[64:67]
	v_mfma_f32_16x16x32_bf16 v[68:71], v[252:255], v[216:219], v[68:71]
	s_mov_b32 m0, s41
	s_add_i32 s51, s50, 0x24000
	v_mfma_f32_16x16x32_bf16 v[60:63], v[252:255], v[220:223], v[60:63]
	buffer_load_dwordx4 v125, s[36:39], s51 offen lds
	v_mfma_f32_16x16x32_bf16 v[56:59], v[248:251], v[220:223], v[56:59]
	ds_read_b128 v[248:251], v121 offset:63488
	ds_read_b128 v[252:255], v121 offset:64512
	s_setprio 1
	s_waitcnt lgkmcnt(8)
	v_mfma_f32_16x16x32_bf16 v[80:83], v[224:227], v[88:91], v[160:163]
	v_mfma_f32_16x16x32_bf16 v[76:79], v[228:231], v[88:91], v[164:167]
	s_mov_b32 m0, s40
	s_add_i32 s51, s50, 0x26000
	v_mfma_f32_16x16x32_bf16 v[72:75], v[228:231], v[92:95], v[164:167]
	buffer_load_dwordx4 v125, s[36:39], s51 offen lds
	v_mfma_f32_16x16x32_bf16 v[84:87], v[224:227], v[92:95], v[160:163]
	ds_read_b128 v[224:227], v126 offset:57344
	ds_read_b128 v[228:231], v126 offset:58368
	s_waitcnt lgkmcnt(8)
	v_mfma_f32_16x16x32_bf16 v[80:83], v[232:235], v[96:99], v[80:83]
	v_cvt_pk_bf16_f32 v0, v64, v65
	v_mfma_f32_16x16x32_bf16 v[76:79], v[236:239], v[96:99], v[76:79]
	v_cvt_pk_bf16_f32 v1, v66, v67
	v_mfma_f32_16x16x32_bf16 v[72:75], v[236:239], v[100:103], v[72:75]
	v_cvt_pk_bf16_f32 v2, v68, v69
	v_mfma_f32_16x16x32_bf16 v[84:87], v[232:235], v[100:103], v[84:87]
	v_cvt_pk_bf16_f32 v3, v70, v71
	ds_read_b128 v[232:235], v126 offset:59392
	ds_read_b128 v[236:239], v126 offset:60416
	s_waitcnt lgkmcnt(6)
	v_mfma_f32_16x16x32_bf16 v[80:83], v[240:243], v[104:107], v[80:83]
	v_cvt_pk_bf16_f32 v4, v56, v57
	v_mfma_f32_16x16x32_bf16 v[76:79], v[244:247], v[104:107], v[76:79]
	v_cvt_pk_bf16_f32 v5, v58, v59
	v_mfma_f32_16x16x32_bf16 v[72:75], v[244:247], v[108:111], v[72:75]
	v_cvt_pk_bf16_f32 v6, v60, v61
	v_mfma_f32_16x16x32_bf16 v[84:87], v[240:243], v[108:111], v[84:87]
	v_cvt_pk_bf16_f32 v7, v62, v63
	ds_read_b128 v[240:243], v126 offset:61440
	ds_read_b128 v[244:247], v126 offset:62464
	s_waitcnt lgkmcnt(6)
	v_mfma_f32_16x16x32_bf16 v[80:83], v[248:251], v[184:187], v[80:83]
	v_pk_max_i16 v0, v0, 0
	v_mfma_f32_16x16x32_bf16 v[76:79], v[252:255], v[184:187], v[76:79]
	v_pk_max_i16 v1, v1, 0
	v_mfma_f32_16x16x32_bf16 v[72:75], v[252:255], v[188:191], v[72:75]
	v_pk_max_i16 v2, v2, 0
	v_mfma_f32_16x16x32_bf16 v[84:87], v[248:251], v[188:191], v[84:87]
	v_pk_max_i16 v3, v3, 0
	ds_read_b128 v[248:251], v126 offset:63488
	ds_read_b128 v[252:255], v126 offset:64512
	s_setprio 0
	s_waitcnt lgkmcnt(6)
	v_mfma_f32_16x16x32_bf16 v[80:83], v[224:227], v[192:195], v[80:83]
	v_pk_max_i16 v4, v4, 0
	v_mfma_f32_16x16x32_bf16 v[76:79], v[228:231], v[192:195], v[76:79]
	v_pk_max_i16 v5, v5, 0
	v_mfma_f32_16x16x32_bf16 v[72:75], v[228:231], v[196:199], v[72:75]
	v_pk_max_i16 v6, v6, 0
	v_mfma_f32_16x16x32_bf16 v[84:87], v[224:227], v[196:199], v[84:87]
	v_pk_max_i16 v7, v7, 0
	s_waitcnt lgkmcnt(4)
	v_mfma_f32_16x16x32_bf16 v[80:83], v[232:235], v[200:203], v[80:83]
	v_mfma_f32_16x16x32_bf16 v[76:79], v[236:239], v[200:203], v[76:79]
	v_mfma_f32_16x16x32_bf16 v[72:75], v[236:239], v[204:207], v[72:75]
	v_mfma_f32_16x16x32_bf16 v[84:87], v[232:235], v[204:207], v[84:87]

.Lnerf_head:
	s_waitcnt lgkmcnt(0)
	v_add_u32_e32 v8, 0x22000, v121
	ds_read_b128 v[224:227], v8 offset:0
	ds_read_b128 v[228:231], v8 offset:1024
	ds_read_b128 v[4:7], v183 offset:1024
	ds_read_b128 v[0:3], v183 offset:1024
	v_mfma_f32_16x16x32_bf16 v[80:83], v[240:243], v[48:51], v[80:83]
	ds_read_b128 v[232:235], v8 offset:2048
	v_mfma_f32_16x16x32_bf16 v[76:79], v[244:247], v[48:51], v[76:79]
	ds_read_b128 v[236:239], v8 offset:3072
	v_mfma_f32_16x16x32_bf16 v[72:75], v[244:247], v[52:55], v[72:75]
	v_mfma_f32_16x16x32_bf16 v[84:87], v[240:243], v[52:55], v[84:87]
	ds_read_b128 v[240:243], v8 offset:4096
	ds_read_b128 v[244:247], v8 offset:5120
	v_mfma_f32_16x16x32_bf16 v[80:83], v[248:251], v[112:115], v[80:83]
	v_mfma_f32_16x16x32_bf16 v[76:79], v[252:255], v[112:115], v[76:79]
	v_mfma_f32_16x16x32_bf16 v[72:75], v[252:255], v[116:119], v[72:75]
	v_mfma_f32_16x16x32_bf16 v[84:87], v[248:251], v[116:119], v[84:87]
	ds_read_b128 v[248:251], v8 offset:6144
	ds_read_b128 v[252:255], v8 offset:7168
	s_waitcnt lgkmcnt(7)
	v_mfma_f32_16x16x32_bf16 v[4:7], v[224:227], v[88:91], v[4:7]
	s_waitcnt lgkmcnt(6)
	v_mfma_f32_16x16x32_bf16 v[0:3], v[224:227], v[92:95], v[0:3]
	v_cvt_pk_bf16_f32 v216, v80, v81
	v_cvt_pk_bf16_f32 v217, v82, v83
	v_mfma_f32_16x16x32_bf16 v[4:7], v[228:231], v[96:99], v[4:7]
	v_cvt_pk_bf16_f32 v218, v76, v77
	v_cvt_pk_bf16_f32 v219, v78, v79
	v_mfma_f32_16x16x32_bf16 v[0:3], v[228:231], v[100:103], v[0:3]
	v_cvt_pk_bf16_f32 v220, v84, v85
	v_cvt_pk_bf16_f32 v221, v86, v87
	s_waitcnt lgkmcnt(5)
	v_mfma_f32_16x16x32_bf16 v[4:7], v[232:235], v[104:107], v[4:7]
	v_cvt_pk_bf16_f32 v222, v72, v73
	v_cvt_pk_bf16_f32 v223, v74, v75
	v_mfma_f32_16x16x32_bf16 v[0:3], v[232:235], v[108:111], v[0:3]
	v_pk_max_i16 v216, v216, 0
	v_pk_max_i16 v217, v217, 0
	s_waitcnt lgkmcnt(4)
	v_mfma_f32_16x16x32_bf16 v[4:7], v[236:239], v[184:187], v[4:7]
	v_pk_max_i16 v218, v218, 0
	v_pk_max_i16 v219, v219, 0
	v_mfma_f32_16x16x32_bf16 v[0:3], v[236:239], v[188:191], v[0:3]
	v_pk_max_i16 v220, v220, 0
	v_pk_max_i16 v221, v221, 0
	s_waitcnt lgkmcnt(3)
	v_mfma_f32_16x16x32_bf16 v[4:7], v[240:243], v[192:195], v[4:7]
	v_pk_max_i16 v222, v222, 0
	v_pk_max_i16 v223, v223, 0
	v_mfma_f32_16x16x32_bf16 v[0:3], v[240:243], v[196:199], v[0:3]
	s_waitcnt lgkmcnt(2)
	v_mfma_f32_16x16x32_bf16 v[4:7], v[244:247], v[200:203], v[4:7]
	v_mfma_f32_16x16x32_bf16 v[0:3], v[244:247], v[204:207], v[0:3]
	s_waitcnt lgkmcnt(1)
	v_mfma_f32_16x16x32_bf16 v[4:7], v[248:251], v[208:211], v[4:7]
	v_mfma_f32_16x16x32_bf16 v[0:3], v[248:251], v[212:215], v[0:3]
	s_nop 1
	s_waitcnt lgkmcnt(0)
	v_mfma_f32_16x16x32_bf16 v[4:7], v[252:255], v[216:219], v[4:7]
	v_mfma_f32_16x16x32_bf16 v[0:3], v[252:255], v[220:223], v[0:3]
	s_nop 7
	s_nop 1
	s_setprio 0
	s_and_saveexec_b64 s[20:21], s[2:3]
	s_cbranch_execz .LBB1_20
	s_nop 4
	v_mul_f32_e32 v6, 0xbfb8aa3b, v6
	v_mul_f32_e32 v7, 0xbfb8aa3b, v7
	v_mul_f32_e32 v4, 0xbfb8aa3b, v4
	v_mul_f32_e32 v5, 0xbfb8aa3b, v5
	v_exp_f32_e32 v6, v6
	v_exp_f32_e32 v7, v7
	v_exp_f32_e32 v4, v4
	v_exp_f32_e32 v5, v5
	s_lshl_b32 s24, s45, 6
	s_add_i32 s47, s43, s24
	s_nop 0
	v_add_f32_e32 v6, 1.0, v6
	v_add_f32_e32 v7, 1.0, v7
	v_add_f32_e32 v4, 1.0, v4
	v_add_f32_e32 v5, 1.0, v5
	v_rcp_f32_e32 v6, v6
	v_rcp_f32_e32 v7, v7
	v_rcp_f32_e32 v4, v4
	v_rcp_f32_e32 v5, v5
	s_mov_b64 s[24:25], -1
	s_nop 0
	s_and_b64 vcc, exec, s[16:17]
	s_cbranch_vccz .LBB1_14
	v_or_b32_e32 v8, s47, v130
	v_lshl_add_u32 v8, v8, 4, v182
	ds_write_b128 v8, v[4:7]
	s_mov_b64 s[24:25], 0
